# blocked fp8 expert-weight layout + sc0 sc1 nt on P0's expert stores
# baseline (speedup 1.0000x reference)
; #define MOE_LOAD(v, it) do { _Pragma("unroll") for (int i_ = 0; i_ < 64; ++i_) v[i_] = __builtin_nontemporal_load((it).src + (size_t)(2 * i_) * (it).stride); } while (0)
;     ...
;         for (int j = 0; j < nmine; j += 2) {
;             const int it1 = gw + (j + 1) * NGW, it2 = gw + (j + 2) * NGW;
;             ib = moe_item(wg, wu, wd, win, wout, wpn, wpd, F.ws, it1 <= last ? it1 : last, F.lane); MOE_LOAD(vb, ib);
;             MOE_PROC(va, ia);
;             ia = moe_item(wg, wu, wd, win, wout, wpn, wpd, F.ws, it2 <= last ? it2 : last, F.lane); MOE_LOAD(va, ia);
;             MOE_PROC(vb, ib);
.LBB0_80:
	s_lshl_b64 s[68:69], s[68:69], 3
	v_lshl_add_u64 v[14:15], v[16:17], 0, s[68:69]
	global_load_dword v87, v[16:17], off nt
	v_lshl_add_u64 v[16:17], v[14:15], 0, s[68:69]
	v_lshl_add_u64 v[30:31], v[16:17], 0, s[68:69]
	v_lshl_add_u64 v[32:33], v[30:31], 0, s[68:69]
	v_lshl_add_u64 v[34:35], v[32:33], 0, s[68:69]
	v_lshl_add_u64 v[36:37], v[34:35], 0, s[68:69]
	v_lshl_add_u64 v[38:39], v[36:37], 0, s[68:69]
	v_lshl_add_u64 v[40:41], v[38:39], 0, s[68:69]
	global_load_dword v92, v[14:15], off nt
	global_load_dword v91, v[16:17], off nt
	global_load_dword v90, v[30:31], off nt
	global_load_dword v89, v[32:33], off nt
	global_load_dword v88, v[34:35], off nt
	global_load_dword v86, v[36:37], off nt
	global_load_dword v85, v[38:39], off nt
	global_load_dword v83, v[40:41], off nt
	v_lshl_add_u64 v[14:15], v[40:41], 0, s[68:69]
	v_lshl_add_u64 v[16:17], v[14:15], 0, s[68:69]
	global_load_dword v84, v[14:15], off nt
	global_load_dword v79, v[16:17], off nt
	v_lshl_add_u64 v[14:15], v[16:17], 0, s[68:69]
	global_load_dword v80, v[14:15], off nt
	v_lshl_add_u64 v[14:15], v[14:15], 0, s[68:69]
	global_load_dword v75, v[14:15], off nt
	v_lshl_add_u64 v[14:15], v[14:15], 0, s[68:69]
	global_load_dword v76, v[14:15], off nt
	v_lshl_add_u64 v[14:15], v[14:15], 0, s[68:69]
	global_load_dword v71, v[14:15], off nt
	v_lshl_add_u64 v[14:15], v[14:15], 0, s[68:69]
	global_load_dword v72, v[14:15], off nt
	v_lshl_add_u64 v[14:15], v[14:15], 0, s[68:69]
	global_load_dword v65, v[14:15], off nt
	v_lshl_add_u64 v[14:15], v[14:15], 0, s[68:69]
	global_load_dword v66, v[14:15], off nt
	v_lshl_add_u64 v[14:15], v[14:15], 0, s[68:69]
	global_load_dword v61, v[14:15], off nt
	v_lshl_add_u64 v[14:15], v[14:15], 0, s[68:69]
	global_load_dword v62, v[14:15], off nt
	v_lshl_add_u64 v[14:15], v[14:15], 0, s[68:69]
	global_load_dword v57, v[14:15], off nt
	v_lshl_add_u64 v[14:15], v[14:15], 0, s[68:69]
	global_load_dword v58, v[14:15], off nt
	v_lshl_add_u64 v[14:15], v[14:15], 0, s[68:69]
	global_load_dword v53, v[14:15], off nt
	v_lshl_add_u64 v[14:15], v[14:15], 0, s[68:69]
	global_load_dword v54, v[14:15], off nt
	v_lshl_add_u64 v[14:15], v[14:15], 0, s[68:69]
	global_load_dword v45, v[14:15], off nt
	v_lshl_add_u64 v[14:15], v[14:15], 0, s[68:69]
	global_load_dword v46, v[14:15], off nt
	v_lshl_add_u64 v[14:15], v[14:15], 0, s[68:69]
	global_load_dword v35, v[14:15], off nt
	v_lshl_add_u64 v[14:15], v[14:15], 0, s[68:69]
	global_load_dword v36, v[14:15], off nt
	v_lshl_add_u64 v[14:15], v[14:15], 0, s[68:69]
	global_load_dword v33, v[14:15], off nt
	v_lshl_add_u64 v[14:15], v[14:15], 0, s[68:69]
	global_load_dword v34, v[14:15], off nt
	v_lshl_add_u64 v[14:15], v[14:15], 0, s[68:69]
	global_load_dword v31, v[14:15], off nt
	v_lshl_add_u64 v[14:15], v[14:15], 0, s[68:69]
	global_load_dword v32, v[14:15], off nt
	v_lshl_add_u64 v[14:15], v[14:15], 0, s[68:69]
	global_load_dword v29, v[14:15], off nt
	v_lshl_add_u64 v[14:15], v[14:15], 0, s[68:69]
	global_load_dword v30, v[14:15], off nt
	v_lshl_add_u64 v[14:15], v[14:15], 0, s[68:69]
	global_load_dword v81, v[14:15], off nt
	v_lshl_add_u64 v[14:15], v[14:15], 0, s[68:69]
	global_load_dword v82, v[14:15], off nt
	v_lshl_add_u64 v[14:15], v[14:15], 0, s[68:69]
	global_load_dword v77, v[14:15], off nt
	v_lshl_add_u64 v[14:15], v[14:15], 0, s[68:69]
	global_load_dword v78, v[14:15], off nt
	v_lshl_add_u64 v[14:15], v[14:15], 0, s[68:69]
	global_load_dword v73, v[14:15], off nt
	v_lshl_add_u64 v[14:15], v[14:15], 0, s[68:69]
	global_load_dword v74, v[14:15], off nt
	v_lshl_add_u64 v[14:15], v[14:15], 0, s[68:69]
	global_load_dword v69, v[14:15], off nt
	v_lshl_add_u64 v[14:15], v[14:15], 0, s[68:69]
	global_load_dword v70, v[14:15], off nt
	v_lshl_add_u64 v[14:15], v[14:15], 0, s[68:69]
	global_load_dword v67, v[14:15], off nt
	v_lshl_add_u64 v[14:15], v[14:15], 0, s[68:69]
	global_load_dword v68, v[14:15], off nt
	v_lshl_add_u64 v[14:15], v[14:15], 0, s[68:69]
	global_load_dword v63, v[14:15], off nt
	v_lshl_add_u64 v[14:15], v[14:15], 0, s[68:69]
	global_load_dword v64, v[14:15], off nt
	v_lshl_add_u64 v[14:15], v[14:15], 0, s[68:69]
	global_load_dword v59, v[14:15], off nt
	v_lshl_add_u64 v[14:15], v[14:15], 0, s[68:69]
	global_load_dword v60, v[14:15], off nt
	v_lshl_add_u64 v[14:15], v[14:15], 0, s[68:69]
	global_load_dword v55, v[14:15], off nt
	v_lshl_add_u64 v[14:15], v[14:15], 0, s[68:69]
	global_load_dword v56, v[14:15], off nt
	v_lshl_add_u64 v[14:15], v[14:15], 0, s[68:69]
	global_load_dword v51, v[14:15], off nt
	v_lshl_add_u64 v[14:15], v[14:15], 0, s[68:69]
	global_load_dword v52, v[14:15], off nt
	v_lshl_add_u64 v[14:15], v[14:15], 0, s[68:69]
	global_load_dword v38, v[14:15], off nt
	v_lshl_add_u64 v[14:15], v[14:15], 0, s[68:69]
	global_load_dword v39, v[14:15], off nt
	v_lshl_add_u64 v[14:15], v[14:15], 0, s[68:69]
	global_load_dword v40, v[14:15], off nt
	v_lshl_add_u64 v[14:15], v[14:15], 0, s[68:69]
	global_load_dword v42, v[14:15], off nt
	v_lshl_add_u64 v[14:15], v[14:15], 0, s[68:69]
	global_load_dword v37, v[14:15], off nt
	v_lshl_add_u64 v[14:15], v[14:15], 0, s[68:69]
	global_load_dword v41, v[14:15], off nt
	v_lshl_add_u64 v[14:15], v[14:15], 0, s[68:69]
	global_load_dword v43, v[14:15], off nt
	v_lshl_add_u64 v[14:15], v[14:15], 0, s[68:69]
	global_load_dword v44, v[14:15], off nt
	v_lshl_add_u64 v[14:15], v[14:15], 0, s[68:69]
	global_load_dword v47, v[14:15], off nt
	v_lshl_add_u64 v[14:15], v[14:15], 0, s[68:69]
	global_load_dword v48, v[14:15], off nt
	v_lshl_add_u64 v[14:15], v[14:15], 0, s[68:69]
	global_load_dword v49, v[14:15], off nt
	v_lshl_add_u64 v[14:15], v[14:15], 0, s[68:69]
	s_waitcnt vmcnt(62)
	ds_write2st64_b32 v28, v93, v101 offset1:1
	ds_write2st64_b32 v28, v99, v100 offset0:2 offset1:3
	ds_write2st64_b32 v28, v97, v98 offset0:4 offset1:5
	ds_write2st64_b32 v28, v95, v96 offset0:6 offset1:7
	ds_write2st64_b32 v21, v94, v124 offset0:8 offset1:9
	ds_write2st64_b32 v21, v104, v114 offset0:10 offset1:11
	ds_write2st64_b32 v21, v105, v115 offset0:12 offset1:13
	ds_write2st64_b32 v21, v106, v116 offset0:14 offset1:15
	ds_write2st64_b32 v22, v107, v117 offset0:16 offset1:17
	ds_write2st64_b32 v22, v108, v118 offset0:18 offset1:19
	ds_write2st64_b32 v22, v109, v119 offset0:20 offset1:21
	ds_write2st64_b32 v22, v110, v120 offset0:22 offset1:23
	ds_write2st64_b32 v23, v111, v121 offset0:24 offset1:25
	ds_write2st64_b32 v23, v112, v122 offset0:26 offset1:27
	global_load_dword v50, v[14:15], off nt
	ds_write2st64_b32 v23, v102, v103 offset0:28 offset1:29
	ds_write2st64_b32 v23, v113, v123 offset0:30 offset1:31
	ds_write2st64_b32 v24, v125, v126 offset0:32 offset1:33
	ds_write2st64_b32 v24, v127, v128 offset0:34 offset1:35
	ds_write2st64_b32 v24, v129, v130 offset0:36 offset1:37
	ds_write2st64_b32 v24, v131, v132 offset0:38 offset1:39
	ds_write2st64_b32 v25, v133, v134 offset0:40 offset1:41
	ds_write2st64_b32 v25, v135, v136 offset0:42 offset1:43
	ds_write2st64_b32 v25, v137, v138 offset0:44 offset1:45
	ds_write2st64_b32 v25, v139, v140 offset0:46 offset1:47
	ds_write2st64_b32 v26, v141, v142 offset0:48 offset1:49
	ds_write2st64_b32 v26, v143, v144 offset0:50 offset1:51
	ds_write2st64_b32 v26, v146, v147 offset0:52 offset1:53
	ds_write2st64_b32 v26, v148, v149 offset0:54 offset1:55
	ds_write2st64_b32 v27, v151, v152 offset0:56 offset1:57
	ds_write2st64_b32 v27, v153, v154 offset0:58 offset1:59
	ds_write2st64_b32 v27, v155, v157 offset0:60 offset1:61
	ds_write2st64_b32 v27, v158, v159 offset0:62 offset1:63
	s_waitcnt lgkmcnt(0)
	ds_read2_b32 v[16:17], v1 offset1:32
	v_lshlrev_b64 v[14:15], s44, v[2:3]
	v_lshl_add_u64 v[12:13], v[12:13], 0, v[14:15]
	v_lshl_add_u64 v[98:99], v[12:13], 0, v[6:7]
	v_mov_b32_e32 v12, 0
	s_waitcnt lgkmcnt(0)
	v_mul_f32_e32 v4, 0x42800000, v16
	v_mul_f32_e32 v13, 0x42800000, v17
	ds_read2_b32 v[16:17], v1 offset0:64 offset1:96
	ds_read2_b32 v[94:95], v1 offset0:128 offset1:160
	v_cvt_pk_fp8_f32 v12, v4, v13
	v_lshlrev_b64 v[14:15], s46, v[2:3]
	v_lshl_add_u64 v[10:11], v[10:11], 0, v[14:15]
	s_waitcnt lgkmcnt(1)
	v_mul_f32_e32 v4, 0x42800000, v16
	v_mul_f32_e32 v13, 0x42800000, v17
	v_cvt_pk_fp8_f32 v12, v4, v13 op_sel:[0,0,1]
	s_waitcnt lgkmcnt(0)
	v_mul_f32_e32 v4, 0x42800000, v94
	ds_read2_b32 v[14:15], v1 offset0:192 offset1:224
	v_mul_f32_e32 v16, 0x42800000, v95
	v_mov_b32_e32 v13, 0
	v_cvt_pk_fp8_f32 v13, v4, v16
	ds_read2_b32 v[16:17], v145 offset1:32
	s_waitcnt lgkmcnt(1)
	v_mul_f32_e32 v4, 0x42800000, v14
	v_mul_f32_e32 v93, 0x42800000, v15
	ds_read2_b32 v[14:15], v145 offset0:64 offset1:96
	v_cvt_pk_fp8_f32 v13, v4, v93 op_sel:[0,0,1]
	s_waitcnt lgkmcnt(1)
	v_mul_f32_e32 v4, 0x42800000, v16
	v_mul_f32_e32 v93, 0x42800000, v17
	ds_read2_b32 v[16:17], v145 offset0:128 offset1:160
	s_waitcnt lgkmcnt(1)
	v_mul_f32_e32 v96, 0x42800000, v14
	v_mov_b32_e32 v14, 0
	v_cvt_pk_fp8_f32 v14, v4, v93
	v_mul_f32_e32 v97, 0x42800000, v15
	s_waitcnt lgkmcnt(0)
	v_mul_f32_e32 v4, 0x42800000, v16
	v_mul_f32_e32 v93, 0x42800000, v17
	ds_read2_b32 v[16:17], v145 offset0:192 offset1:224
	v_mov_b32_e32 v15, 0
	v_cvt_pk_fp8_f32 v15, v4, v93
	ds_read2_b32 v[94:95], v9 offset1:32
	v_cvt_pk_fp8_f32 v14, v96, v97 op_sel:[0,0,1]
	s_waitcnt lgkmcnt(1)
	v_mul_f32_e32 v4, 0x42800000, v16
	v_mul_f32_e32 v16, 0x42800000, v17
	v_cvt_pk_fp8_f32 v15, v4, v16 op_sel:[0,0,1]
	ds_read2_b32 v[16:17], v9 offset0:64 offset1:96
	s_waitcnt lgkmcnt(1)
	v_mul_f32_e32 v4, 0x42800000, v94
	v_mul_f32_e32 v93, 0x42800000, v95
	v_mov_b32_e32 v94, 0
	ds_read2_b32 v[96:97], v9 offset0:128 offset1:160
	v_cvt_pk_fp8_f32 v94, v4, v93
	global_store_dwordx4 v[98:99], v[12:15], off sc0 sc1 nt
	s_waitcnt lgkmcnt(1)
	v_mul_f32_e32 v4, 0x42800000, v16
	v_mov_b32_e32 v95, 0
	v_mul_f32_e32 v12, 0x42800000, v17
	v_cvt_pk_fp8_f32 v94, v4, v12 op_sel:[0,0,1]
	s_waitcnt lgkmcnt(0)
	v_mul_f32_e32 v4, 0x42800000, v96
	ds_read2_b32 v[12:13], v9 offset0:192 offset1:224
	v_mul_f32_e32 v14, 0x42800000, v97
	v_cvt_pk_fp8_f32 v95, v4, v14
	ds_read2_b32 v[14:15], v150 offset1:32
	v_mov_b32_e32 v96, 0
	s_waitcnt lgkmcnt(1)
; #define MOE_LOAD(v, it) do { _Pragma("unroll") for (int i_ = 0; i_ < 64; ++i_) v[i_] = __builtin_nontemporal_load((it).src + (size_t)(2 * i_) * (it).stride); } while (0)
;     ...
;         for (int j = 0; j < nmine; j += 2) {
;             const int it1 = gw + (j + 1) * NGW, it2 = gw + (j + 2) * NGW;
;             ib = moe_item(wg, wu, wd, win, wout, wpn, wpd, F.ws, it1 <= last ? it1 : last, F.lane); MOE_LOAD(vb, ib);
;             MOE_PROC(va, ia);
;             ia = moe_item(wg, wu, wd, win, wout, wpn, wpd, F.ws, it2 <= last ? it2 : last, F.lane); MOE_LOAD(va, ia);
;             MOE_PROC(vb, ib);
;         }
	v_mul_f32_e32 v4, 0x42800000, v12
	v_mul_f32_e32 v16, 0x42800000, v13
	ds_read2_b32 v[12:13], v150 offset0:64 offset1:96
	v_cvt_pk_fp8_f32 v95, v4, v16 op_sel:[0,0,1]
	s_waitcnt lgkmcnt(1)
	v_mul_f32_e32 v4, 0x42800000, v14
	v_mul_f32_e32 v16, 0x42800000, v15
	ds_read2_b32 v[14:15], v150 offset0:128 offset1:160
	s_waitcnt lgkmcnt(1)
	v_mul_f32_e32 v17, 0x42800000, v12
	v_mul_f32_e32 v93, 0x42800000, v13
	ds_read2_b32 v[12:13], v150 offset0:192 offset1:224
	v_cvt_pk_fp8_f32 v96, v4, v16
	s_waitcnt lgkmcnt(1)
	v_mul_f32_e32 v4, 0x42800000, v14
	v_mul_f32_e32 v14, 0x42800000, v15
	v_mov_b32_e32 v97, 0
	v_cvt_pk_fp8_f32 v97, v4, v14
	s_waitcnt lgkmcnt(0)
	v_mul_f32_e32 v4, 0x42800000, v12
	v_mul_f32_e32 v12, 0x42800000, v13
	v_cvt_pk_fp8_f32 v96, v17, v93 op_sel:[0,0,1]
	v_cvt_pk_fp8_f32 v97, v4, v12 op_sel:[0,0,1]
	s_lshl_b32 s4, s42, 3
	ds_read2_b32 v[12:13], v18 offset1:32
	v_lshl_add_u64 v[16:17], v[98:99], 0, s[4:5]
	ds_read2_b32 v[14:15], v18 offset0:64 offset1:96
	global_store_dwordx4 v[16:17], v[94:97], off sc0 sc1 nt
	ds_read2_b32 v[94:95], v18 offset0:128 offset1:160
	s_waitcnt lgkmcnt(2)
	v_mul_f32_e32 v4, 0x42800000, v12
	v_mul_f32_e32 v13, 0x42800000, v13
	v_mov_b32_e32 v12, 0
	s_waitcnt lgkmcnt(1)
	v_mul_f32_e32 v93, 0x42800000, v14
	v_mul_f32_e32 v96, 0x42800000, v15
	v_cvt_pk_fp8_f32 v12, v4, v13
	s_waitcnt lgkmcnt(0)
	v_mul_f32_e32 v4, 0x42800000, v94
	v_mul_f32_e32 v94, 0x42800000, v95
	ds_read2_b32 v[14:15], v18 offset0:192 offset1:224
	v_mov_b32_e32 v13, 0
	v_cvt_pk_fp8_f32 v13, v4, v94
	ds_read2_b32 v[94:95], v156 offset1:32
	v_cvt_pk_fp8_f32 v12, v93, v96 op_sel:[0,0,1]
	s_waitcnt lgkmcnt(1)
	v_mul_f32_e32 v4, 0x42800000, v14
	v_mul_f32_e32 v14, 0x42800000, v15
	ds_read2_b32 v[96:97], v156 offset0:64 offset1:96
	v_cvt_pk_fp8_f32 v13, v4, v14 op_sel:[0,0,1]
	s_waitcnt lgkmcnt(1)
	v_mul_f32_e32 v4, 0x42800000, v94
	v_mul_f32_e32 v15, 0x42800000, v95
	v_mov_b32_e32 v14, 0
	ds_read2_b32 v[94:95], v156 offset0:128 offset1:160
	v_cvt_pk_fp8_f32 v14, v4, v15
	s_waitcnt lgkmcnt(1)
	v_mul_f32_e32 v4, 0x42800000, v96
	v_mul_f32_e32 v15, 0x42800000, v97
	ds_read2_b32 v[96:97], v156 offset0:192 offset1:224
	v_cvt_pk_fp8_f32 v14, v4, v15 op_sel:[0,0,1]
	s_waitcnt lgkmcnt(1)
	v_mul_f32_e32 v4, 0x42800000, v94
	v_mul_f32_e32 v93, 0x42800000, v95
	ds_read2_b32 v[94:95], v19 offset1:32
	s_waitcnt lgkmcnt(1)
	v_mul_f32_e32 v100, 0x42800000, v96
	v_mul_f32_e32 v101, 0x42800000, v97
	v_mov_b32_e32 v15, 0
	ds_read2_b32 v[96:97], v19 offset0:64 offset1:96
	v_cvt_pk_fp8_f32 v15, v4, v93
	s_waitcnt lgkmcnt(1)
	v_mul_f32_e32 v4, 0x42800000, v94
	v_mul_f32_e32 v93, 0x42800000, v95
	v_mov_b32_e32 v94, 0
	ds_read2_b32 v[98:99], v19 offset0:128 offset1:160
	v_cvt_pk_fp8_f32 v94, v4, v93
	s_waitcnt lgkmcnt(1)
	v_mul_f32_e32 v4, 0x42800000, v96
	v_mul_f32_e32 v93, 0x42800000, v97
	ds_read2_b32 v[96:97], v19 offset0:192 offset1:224
	v_cvt_pk_fp8_f32 v94, v4, v93 op_sel:[0,0,1]
	s_waitcnt lgkmcnt(1)
	v_mul_f32_e32 v4, 0x42800000, v98
	v_mul_f32_e32 v93, 0x42800000, v99
	v_mov_b32_e32 v95, 0
	ds_read2_b32 v[98:99], v160 offset1:32
	v_cvt_pk_fp8_f32 v95, v4, v93
	s_waitcnt lgkmcnt(1)
	v_mul_f32_e32 v4, 0x42800000, v96
	v_mul_f32_e32 v93, 0x42800000, v97
	ds_read2_b32 v[96:97], v160 offset0:64 offset1:96
	v_cvt_pk_fp8_f32 v95, v4, v93 op_sel:[0,0,1]
	s_waitcnt lgkmcnt(1)
	v_mul_f32_e32 v4, 0x42800000, v98
	v_mul_f32_e32 v93, 0x42800000, v99
	ds_read2_b32 v[98:99], v160 offset0:128 offset1:160
	v_cvt_pk_fp8_f32 v15, v100, v101 op_sel:[0,0,1]
	s_waitcnt lgkmcnt(1)
	v_mul_f32_e32 v102, 0x42800000, v96
	v_mov_b32_e32 v96, 0
	ds_read2_b32 v[100:101], v160 offset0:192 offset1:224
	v_mul_f32_e32 v103, 0x42800000, v97
	v_cvt_pk_fp8_f32 v96, v4, v93
	s_waitcnt lgkmcnt(1)
	v_mul_f32_e32 v4, 0x42800000, v98
	v_mul_f32_e32 v93, 0x42800000, v99
	v_mov_b32_e32 v97, 0
	v_cvt_pk_fp8_f32 v97, v4, v93
	s_waitcnt lgkmcnt(0)
	v_mul_f32_e32 v4, 0x42800000, v100
	v_mul_f32_e32 v93, 0x42800000, v101
	v_cvt_pk_fp8_f32 v96, v102, v103 op_sel:[0,0,1]
	v_cvt_pk_fp8_f32 v97, v4, v93 op_sel:[0,0,1]
	v_lshl_add_u64 v[16:17], v[16:17], 0, s[4:5]
	global_store_dwordx4 v[16:17], v[12:15], off sc0 sc1 nt
	s_add_i32 s91, s91, 2
	s_cmp_ge_i32 s91, s6
	v_lshl_add_u64 v[12:13], v[16:17], 0, s[4:5]
	global_store_dwordx4 v[12:13], v[94:97], off sc0 sc1 nt
	s_waitcnt lgkmcnt(0)
	s_cbranch_scc1 .LBB0_130

.LBB0_105:
	s_lshl_b64 s[46:47], s[46:47], 3
	global_load_dword v93, v[16:17], off nt
	v_lshl_add_u64 v[16:17], v[16:17], 0, s[46:47]
	v_lshl_add_u64 v[94:95], v[16:17], 0, s[46:47]
	v_lshl_add_u64 v[96:97], v[94:95], 0, s[46:47]
	v_lshl_add_u64 v[102:103], v[96:97], 0, s[46:47]
	v_lshl_add_u64 v[104:105], v[102:103], 0, s[46:47]
	v_lshl_add_u64 v[106:107], v[104:105], 0, s[46:47]
	v_lshl_add_u64 v[108:109], v[106:107], 0, s[46:47]
	v_lshl_add_u64 v[110:111], v[108:109], 0, s[46:47]
	global_load_dword v101, v[16:17], off nt
	global_load_dword v99, v[94:95], off nt
	global_load_dword v100, v[96:97], off nt
	s_nop 0
	global_load_dword v97, v[102:103], off nt
	global_load_dword v98, v[104:105], off nt
	global_load_dword v95, v[106:107], off nt
	global_load_dword v96, v[108:109], off nt
	global_load_dword v94, v[110:111], off nt
	v_lshl_add_u64 v[16:17], v[110:111], 0, s[46:47]
	s_waitcnt vmcnt(9)
	ds_write2st64_b32 v28, v87, v92 offset1:1
	v_lshl_add_u64 v[102:103], v[16:17], 0, s[46:47]
	global_load_dword v124, v[16:17], off nt
	global_load_dword v104, v[102:103], off nt
	v_lshl_add_u64 v[16:17], v[102:103], 0, s[46:47]
	global_load_dword v114, v[16:17], off nt
	v_lshl_add_u64 v[16:17], v[16:17], 0, s[46:47]
	global_load_dword v105, v[16:17], off nt
	v_lshl_add_u64 v[16:17], v[16:17], 0, s[46:47]
	global_load_dword v115, v[16:17], off nt
	v_lshl_add_u64 v[16:17], v[16:17], 0, s[46:47]
	global_load_dword v106, v[16:17], off nt
	v_lshl_add_u64 v[16:17], v[16:17], 0, s[46:47]
	global_load_dword v116, v[16:17], off nt
	v_lshl_add_u64 v[16:17], v[16:17], 0, s[46:47]
	global_load_dword v107, v[16:17], off nt
	v_lshl_add_u64 v[16:17], v[16:17], 0, s[46:47]
	global_load_dword v117, v[16:17], off nt
	v_lshl_add_u64 v[16:17], v[16:17], 0, s[46:47]
	global_load_dword v108, v[16:17], off nt
	v_lshl_add_u64 v[16:17], v[16:17], 0, s[46:47]
	global_load_dword v118, v[16:17], off nt
	v_lshl_add_u64 v[16:17], v[16:17], 0, s[46:47]
	global_load_dword v109, v[16:17], off nt
	v_lshl_add_u64 v[16:17], v[16:17], 0, s[46:47]
	global_load_dword v119, v[16:17], off nt
	v_lshl_add_u64 v[16:17], v[16:17], 0, s[46:47]
	global_load_dword v110, v[16:17], off nt
	v_lshl_add_u64 v[16:17], v[16:17], 0, s[46:47]
	global_load_dword v120, v[16:17], off nt
	v_lshl_add_u64 v[16:17], v[16:17], 0, s[46:47]
	global_load_dword v111, v[16:17], off nt
	v_lshl_add_u64 v[16:17], v[16:17], 0, s[46:47]
	global_load_dword v121, v[16:17], off nt
	v_lshl_add_u64 v[16:17], v[16:17], 0, s[46:47]
	global_load_dword v112, v[16:17], off nt
	v_lshl_add_u64 v[16:17], v[16:17], 0, s[46:47]
	global_load_dword v122, v[16:17], off nt
	v_lshl_add_u64 v[16:17], v[16:17], 0, s[46:47]
	global_load_dword v102, v[16:17], off nt
	v_lshl_add_u64 v[16:17], v[16:17], 0, s[46:47]
	global_load_dword v103, v[16:17], off nt
	v_lshl_add_u64 v[16:17], v[16:17], 0, s[46:47]
	global_load_dword v113, v[16:17], off nt
	v_lshl_add_u64 v[16:17], v[16:17], 0, s[46:47]
	global_load_dword v123, v[16:17], off nt
	v_lshl_add_u64 v[16:17], v[16:17], 0, s[46:47]
	global_load_dword v125, v[16:17], off nt
	v_lshl_add_u64 v[16:17], v[16:17], 0, s[46:47]
	global_load_dword v126, v[16:17], off nt
	v_lshl_add_u64 v[16:17], v[16:17], 0, s[46:47]
	global_load_dword v127, v[16:17], off nt
	v_lshl_add_u64 v[16:17], v[16:17], 0, s[46:47]
	global_load_dword v128, v[16:17], off nt
	v_lshl_add_u64 v[16:17], v[16:17], 0, s[46:47]
	global_load_dword v129, v[16:17], off nt
	v_lshl_add_u64 v[16:17], v[16:17], 0, s[46:47]
	global_load_dword v130, v[16:17], off nt
	v_lshl_add_u64 v[16:17], v[16:17], 0, s[46:47]
	global_load_dword v131, v[16:17], off nt
	v_lshl_add_u64 v[16:17], v[16:17], 0, s[46:47]
	global_load_dword v132, v[16:17], off nt
	v_lshl_add_u64 v[16:17], v[16:17], 0, s[46:47]
	global_load_dword v133, v[16:17], off nt
	v_lshl_add_u64 v[16:17], v[16:17], 0, s[46:47]
	global_load_dword v134, v[16:17], off nt
	v_lshl_add_u64 v[16:17], v[16:17], 0, s[46:47]
	global_load_dword v135, v[16:17], off nt
	v_lshl_add_u64 v[16:17], v[16:17], 0, s[46:47]
	global_load_dword v136, v[16:17], off nt
	v_lshl_add_u64 v[16:17], v[16:17], 0, s[46:47]
	global_load_dword v137, v[16:17], off nt
	v_lshl_add_u64 v[16:17], v[16:17], 0, s[46:47]
	global_load_dword v138, v[16:17], off nt
	v_lshl_add_u64 v[16:17], v[16:17], 0, s[46:47]
	global_load_dword v139, v[16:17], off nt
	v_lshl_add_u64 v[16:17], v[16:17], 0, s[46:47]
	global_load_dword v140, v[16:17], off nt
	v_lshl_add_u64 v[16:17], v[16:17], 0, s[46:47]
	global_load_dword v141, v[16:17], off nt
	v_lshl_add_u64 v[16:17], v[16:17], 0, s[46:47]
	global_load_dword v142, v[16:17], off nt
	v_lshl_add_u64 v[16:17], v[16:17], 0, s[46:47]
	global_load_dword v143, v[16:17], off nt
	v_lshl_add_u64 v[16:17], v[16:17], 0, s[46:47]
	global_load_dword v144, v[16:17], off nt
	v_lshl_add_u64 v[16:17], v[16:17], 0, s[46:47]
	global_load_dword v146, v[16:17], off nt
	v_lshl_add_u64 v[16:17], v[16:17], 0, s[46:47]
	global_load_dword v147, v[16:17], off nt
	v_lshl_add_u64 v[16:17], v[16:17], 0, s[46:47]
	global_load_dword v148, v[16:17], off nt
	v_lshl_add_u64 v[16:17], v[16:17], 0, s[46:47]
	global_load_dword v149, v[16:17], off nt
	v_lshl_add_u64 v[16:17], v[16:17], 0, s[46:47]
	global_load_dword v151, v[16:17], off nt
	v_lshl_add_u64 v[16:17], v[16:17], 0, s[46:47]
	global_load_dword v152, v[16:17], off nt
	v_lshl_add_u64 v[16:17], v[16:17], 0, s[46:47]
	global_load_dword v153, v[16:17], off nt
	v_lshl_add_u64 v[16:17], v[16:17], 0, s[46:47]
	global_load_dword v154, v[16:17], off nt
	v_lshl_add_u64 v[16:17], v[16:17], 0, s[46:47]
	global_load_dword v155, v[16:17], off nt
	v_lshl_add_u64 v[16:17], v[16:17], 0, s[46:47]
	global_load_dword v157, v[16:17], off nt
	v_lshl_add_u64 v[16:17], v[16:17], 0, s[46:47]
	global_load_dword v158, v[16:17], off nt
	v_lshl_add_u64 v[16:17], v[16:17], 0, s[46:47]
	ds_write2st64_b32 v28, v91, v90 offset0:2 offset1:3
	ds_write2st64_b32 v28, v89, v88 offset0:4 offset1:5
	ds_write2st64_b32 v28, v86, v85 offset0:6 offset1:7
	ds_write2st64_b32 v21, v83, v84 offset0:8 offset1:9
	ds_write2st64_b32 v21, v79, v80 offset0:10 offset1:11
	ds_write2st64_b32 v21, v75, v76 offset0:12 offset1:13
	ds_write2st64_b32 v21, v71, v72 offset0:14 offset1:15
	ds_write2st64_b32 v22, v65, v66 offset0:16 offset1:17
	ds_write2st64_b32 v22, v61, v62 offset0:18 offset1:19
	ds_write2st64_b32 v22, v57, v58 offset0:20 offset1:21
	ds_write2st64_b32 v22, v53, v54 offset0:22 offset1:23
	ds_write2st64_b32 v23, v45, v46 offset0:24 offset1:25
	ds_write2st64_b32 v23, v35, v36 offset0:26 offset1:27
	ds_write2st64_b32 v23, v33, v34 offset0:28 offset1:29
	ds_write2st64_b32 v23, v31, v32 offset0:30 offset1:31
	ds_write2st64_b32 v24, v29, v30 offset0:32 offset1:33
	ds_write2st64_b32 v24, v81, v82 offset0:34 offset1:35
	ds_write2st64_b32 v24, v77, v78 offset0:36 offset1:37
	ds_write2st64_b32 v24, v73, v74 offset0:38 offset1:39
	ds_write2st64_b32 v25, v69, v70 offset0:40 offset1:41
	ds_write2st64_b32 v25, v67, v68 offset0:42 offset1:43
	ds_write2st64_b32 v25, v63, v64 offset0:44 offset1:45
	ds_write2st64_b32 v25, v59, v60 offset0:46 offset1:47
	ds_write2st64_b32 v26, v55, v56 offset0:48 offset1:49
	ds_write2st64_b32 v26, v51, v52 offset0:50 offset1:51
	global_load_dword v159, v[16:17], off nt
	ds_write2st64_b32 v26, v38, v39 offset0:52 offset1:53
	ds_write2st64_b32 v26, v40, v42 offset0:54 offset1:55
	ds_write2st64_b32 v27, v37, v41 offset0:56 offset1:57
	ds_write2st64_b32 v27, v43, v44 offset0:58 offset1:59
	ds_write2st64_b32 v27, v47, v48 offset0:60 offset1:61
	ds_write2st64_b32 v27, v49, v50 offset0:62 offset1:63
	s_waitcnt lgkmcnt(0)
	ds_read2_b32 v[16:17], v1 offset1:32
	v_mov_b32_e32 v30, 0
	ds_read2_b32 v[32:33], v1 offset0:128 offset1:160
	v_mov_b32_e32 v31, 0
	v_add_u32_e32 v145, 0x400, v1
	s_waitcnt lgkmcnt(1)
	v_mul_f32_e32 v4, 0x42800000, v16
	v_mul_f32_e32 v15, 0x42800000, v17
	ds_read2_b32 v[16:17], v1 offset0:64 offset1:96
	v_cvt_pk_fp8_f32 v30, v4, v15
	ds_read2_b32 v[34:35], v145 offset0:128 offset1:160
	v_add_u32_e32 v150, 0x400, v9
	ds_read2_b32 v[38:39], v150 offset0:128 offset1:160
	s_waitcnt lgkmcnt(2)
	v_mul_f32_e32 v4, 0x42800000, v16
	v_mul_f32_e32 v15, 0x42800000, v17
	ds_read2_b32 v[16:17], v1 offset0:192 offset1:224
	v_cvt_pk_fp8_f32 v30, v4, v15 op_sel:[0,0,1]
	v_mul_f32_e32 v4, 0x42800000, v32
	v_mul_f32_e32 v15, 0x42800000, v33
	v_cvt_pk_fp8_f32 v31, v4, v15
	s_waitcnt lgkmcnt(0)
	v_mul_f32_e32 v4, 0x42800000, v16
	v_mul_f32_e32 v15, 0x42800000, v17
	ds_read2_b32 v[16:17], v145 offset0:64 offset1:96
	ds_read2_b32 v[32:33], v145 offset1:32
	v_cvt_pk_fp8_f32 v31, v4, v15 op_sel:[0,0,1]
	v_lshl_add_u64 v[10:11], v[10:11], 0, v[6:7]
	v_add_u32_e32 v156, 0x400, v18
	s_waitcnt lgkmcnt(1)
	v_mul_f32_e32 v29, 0x42800000, v16
	v_mul_f32_e32 v36, 0x42800000, v17
	ds_read2_b32 v[16:17], v145 offset0:192 offset1:224
	s_waitcnt lgkmcnt(1)
	v_mul_f32_e32 v4, 0x42800000, v32
	v_mul_f32_e32 v15, 0x42800000, v33
	v_mov_b32_e32 v32, 0
	v_cvt_pk_fp8_f32 v32, v4, v15
	v_mul_f32_e32 v4, 0x42800000, v34
	v_mul_f32_e32 v15, 0x42800000, v35
	v_mov_b32_e32 v33, 0
	ds_read2_b32 v[34:35], v9 offset1:32
	v_cvt_pk_fp8_f32 v33, v4, v15
	s_waitcnt lgkmcnt(1)
	v_mul_f32_e32 v4, 0x42800000, v16
	v_mul_f32_e32 v15, 0x42800000, v17
	ds_read2_b32 v[16:17], v9 offset0:64 offset1:96
	v_cvt_pk_fp8_f32 v32, v29, v36 op_sel:[0,0,1]
	ds_read2_b32 v[36:37], v9 offset0:128 offset1:160
	v_cvt_pk_fp8_f32 v33, v4, v15 op_sel:[0,0,1]
	s_waitcnt lgkmcnt(2)
	v_mul_f32_e32 v4, 0x42800000, v34
	v_mul_f32_e32 v15, 0x42800000, v35
	v_mov_b32_e32 v34, 0
	v_cvt_pk_fp8_f32 v34, v4, v15
	s_waitcnt lgkmcnt(1)
	v_mul_f32_e32 v4, 0x42800000, v16
	v_mul_f32_e32 v15, 0x42800000, v17
	ds_read2_b32 v[16:17], v9 offset0:192 offset1:224
	s_waitcnt lgkmcnt(1)
	v_mul_f32_e32 v29, 0x42800000, v36
	v_mul_f32_e32 v36, 0x42800000, v37
	v_mov_b32_e32 v35, 0
	v_cvt_pk_fp8_f32 v35, v29, v36
	ds_read2_b32 v[36:37], v150 offset1:32
	v_cvt_pk_fp8_f32 v34, v4, v15 op_sel:[0,0,1]
	s_waitcnt lgkmcnt(1)
	v_mul_f32_e32 v4, 0x42800000, v16
	v_mul_f32_e32 v15, 0x42800000, v17
	ds_read2_b32 v[16:17], v150 offset0:64 offset1:96
	v_cvt_pk_fp8_f32 v35, v4, v15 op_sel:[0,0,1]
	s_waitcnt lgkmcnt(1)
	v_mul_f32_e32 v4, 0x42800000, v36
	v_mul_f32_e32 v15, 0x42800000, v37
	v_mov_b32_e32 v36, 0
	v_cvt_pk_fp8_f32 v36, v4, v15
	s_waitcnt lgkmcnt(0)
	v_mul_f32_e32 v4, 0x42800000, v16
	v_mul_f32_e32 v15, 0x42800000, v17
	ds_read2_b32 v[16:17], v150 offset0:192 offset1:224
	v_cvt_pk_fp8_f32 v36, v4, v15 op_sel:[0,0,1]
	v_mul_f32_e32 v4, 0x42800000, v38
	v_mul_f32_e32 v15, 0x42800000, v39
	v_mov_b32_e32 v37, 0
	v_cvt_pk_fp8_f32 v37, v4, v15
	s_waitcnt lgkmcnt(0)
; __device__ __forceinline__ MoeItem moe_item(const float* wg, const float* wu, const float* wd, const float* win, const float* wout, const float* wpn, const float* wpd, unsigned char* ws, int r, int lane) {
;     ...
;     const int mat = r / MOE_IE, q = r % MOE_IE, e = mat / 3, which = mat % 3, kb = q / 64, nb = q % 64, n0 = nb * 32;
;     const float* src = (which == 0 ? wg : (which == 1 ? wu : wd)) + (size_t)e * DM * DFF + (size_t)(kb * 128 + (lane >> 5)) * DFF + n0 + (lane & 31);
;     unsigned char* dst;
;     if (which < 2) dst = ws + WS_WGUT + ((size_t)(e * 16 + (n0 >> 7)) * 256 + which * 128 + (n0 & 127)) * DM;
;     else dst = ws + WS_WDT + ((size_t)e * DM + n0) * DFF;
;     MoeItem it; it.stride = DFF; it.dpitch = DM; it.src = src; it.dst = dst + kb * 128 + (size_t)(lane >> 3) * DM + 16 * (lane & 7); return it;
	v_mul_f32_e32 v4, 0x42800000, v16
	v_mul_f32_e32 v15, 0x42800000, v17
	ds_read2_b32 v[16:17], v18 offset1:32
	v_cvt_pk_fp8_f32 v37, v4, v15 op_sel:[0,0,1]
	global_store_dwordx4 v[10:11], v[30:33], off sc0 sc1 nt
	ds_read2_b32 v[32:33], v18 offset0:64 offset1:96
	s_lshl_b64 s[38:39], s[38:39], 3
	s_waitcnt lgkmcnt(1)
	v_mul_f32_e32 v4, 0x42800000, v16
	v_mul_f32_e32 v15, 0x42800000, v17
	ds_read2_b32 v[16:17], v18 offset0:128 offset1:160
	v_mov_b32_e32 v30, 0
	v_cvt_pk_fp8_f32 v30, v4, v15
	s_waitcnt lgkmcnt(1)
	v_mul_f32_e32 v4, 0x42800000, v32
	v_mov_b32_e32 v31, 0
	s_waitcnt lgkmcnt(0)
	v_mul_f32_e32 v29, 0x42800000, v16
	v_mul_f32_e32 v32, 0x42800000, v17
	ds_read2_b32 v[16:17], v18 offset0:192 offset1:224
	v_mul_f32_e32 v15, 0x42800000, v33
	v_cvt_pk_fp8_f32 v31, v29, v32
	ds_read2_b32 v[32:33], v156 offset1:32
	v_cvt_pk_fp8_f32 v30, v4, v15 op_sel:[0,0,1]
	s_waitcnt lgkmcnt(1)
	v_mul_f32_e32 v4, 0x42800000, v16
	v_mul_f32_e32 v15, 0x42800000, v17
	ds_read2_b32 v[16:17], v156 offset0:64 offset1:96
	v_lshl_add_u64 v[10:11], v[10:11], 0, s[38:39]
	global_store_dwordx4 v[10:11], v[34:37], off sc0 sc1 nt
	ds_read2_b32 v[34:35], v156 offset0:128 offset1:160
	v_cvt_pk_fp8_f32 v31, v4, v15 op_sel:[0,0,1]
	s_waitcnt lgkmcnt(2)
	v_mul_f32_e32 v4, 0x42800000, v32
	v_mul_f32_e32 v15, 0x42800000, v33
	v_mov_b32_e32 v32, 0
	v_cvt_pk_fp8_f32 v32, v4, v15
	s_waitcnt lgkmcnt(1)
	v_mul_f32_e32 v4, 0x42800000, v16
	v_mul_f32_e32 v15, 0x42800000, v17
	ds_read2_b32 v[16:17], v156 offset0:192 offset1:224
	s_waitcnt lgkmcnt(1)
	v_mul_f32_e32 v29, 0x42800000, v34
	v_mul_f32_e32 v34, 0x42800000, v35
	v_mov_b32_e32 v33, 0
	v_cvt_pk_fp8_f32 v33, v29, v34
	ds_read2_b32 v[34:35], v19 offset1:32
	v_cvt_pk_fp8_f32 v32, v4, v15 op_sel:[0,0,1]
	s_waitcnt lgkmcnt(1)
	v_mul_f32_e32 v4, 0x42800000, v16
	v_mul_f32_e32 v15, 0x42800000, v17
	ds_read2_b32 v[16:17], v19 offset0:64 offset1:96
	ds_read2_b32 v[36:37], v19 offset0:128 offset1:160
	v_cvt_pk_fp8_f32 v33, v4, v15 op_sel:[0,0,1]
	s_waitcnt lgkmcnt(2)
	v_mul_f32_e32 v4, 0x42800000, v34
	v_mul_f32_e32 v15, 0x42800000, v35
	v_mov_b32_e32 v34, 0
	v_cvt_pk_fp8_f32 v34, v4, v15
	s_waitcnt lgkmcnt(1)
	v_mul_f32_e32 v4, 0x42800000, v16
	v_mul_f32_e32 v15, 0x42800000, v17
	ds_read2_b32 v[16:17], v19 offset0:192 offset1:224
	s_waitcnt lgkmcnt(1)
	v_mul_f32_e32 v29, 0x42800000, v36
	v_mul_f32_e32 v36, 0x42800000, v37
	v_mov_b32_e32 v35, 0
	v_add_u32_e32 v160, 0x400, v19
	v_cvt_pk_fp8_f32 v35, v29, v36
	ds_read2_b32 v[36:37], v160 offset1:32
	v_cvt_pk_fp8_f32 v34, v4, v15 op_sel:[0,0,1]
	s_waitcnt lgkmcnt(1)
	v_mul_f32_e32 v4, 0x42800000, v16
	v_mul_f32_e32 v15, 0x42800000, v17
	ds_read2_b32 v[16:17], v160 offset0:64 offset1:96
	ds_read2_b32 v[38:39], v160 offset0:128 offset1:160
	v_cvt_pk_fp8_f32 v35, v4, v15 op_sel:[0,0,1]
	s_waitcnt lgkmcnt(2)
	v_mul_f32_e32 v4, 0x42800000, v36
	v_mul_f32_e32 v15, 0x42800000, v37
	v_mov_b32_e32 v36, 0
	v_cvt_pk_fp8_f32 v36, v4, v15
	s_waitcnt lgkmcnt(1)
	v_mul_f32_e32 v4, 0x42800000, v16
	v_mul_f32_e32 v15, 0x42800000, v17
	ds_read2_b32 v[16:17], v160 offset0:192 offset1:224
	s_waitcnt lgkmcnt(1)
	v_mul_f32_e32 v29, 0x42800000, v38
	v_mul_f32_e32 v38, 0x42800000, v39
	v_mov_b32_e32 v37, 0
	v_cvt_pk_fp8_f32 v37, v29, v38
	v_cvt_pk_fp8_f32 v36, v4, v15 op_sel:[0,0,1]
	s_waitcnt lgkmcnt(0)
	v_mul_f32_e32 v4, 0x42800000, v16
	v_mul_f32_e32 v15, 0x42800000, v17
	v_cvt_pk_fp8_f32 v37, v4, v15 op_sel:[0,0,1]
	v_lshl_add_u64 v[10:11], v[10:11], 0, s[38:39]
	global_store_dwordx4 v[10:11], v[30:33], off sc0 sc1 nt
	v_lshl_add_u64 v[10:11], v[10:11], 0, s[38:39]
	global_store_dwordx4 v[10:11], v[34:37], off sc0 sc1 nt
	s_waitcnt lgkmcnt(0)
	s_add_i32 s3, s89, s3
	s_mov_b32 s96, 0
	s_min_i32 s43, s3, s7
	s_cmp_lt_i32 s43, 0x19000
	s_mov_b64 s[38:39], -1
	s_cbranch_scc0 .LBB0_126
	s_cmp_lt_i32 s43, 0x18c00
	s_cbranch_scc0 .LBB0_123
	s_cmp_lt_i32 s43, 0x18000
	s_cbranch_scc0 .LBB0_113
	s_mov_b32 s96, 1
	s_ashr_i32 s4, s43, 31
	s_lshr_b32 s4, s4, 22
	s_add_i32 s4, s43, s4
	s_ashr_i32 s39, s4, 10
	s_and_b32 s4, s4, 0xfc00
	s_sub_i32 s46, s43, s4
	s_mul_hi_i32 s4, s43, 0x2aaaaaab
	s_lshr_b32 s38, s4, 31
	s_ashr_i32 s4, s4, 9
	s_add_i32 s38, s4, s38
	s_mul_hi_i32 s4, s39, 0x55555556
	s_lshr_b32 s45, s4, 31
	s_add_i32 s4, s4, s45
	s_mul_i32 s4, s4, 3
	s_sub_i32 s4, s39, s4
	s_sext_i32_i16 s39, s46
	s_bfe_u32 s39, s39, 0x60019
	s_add_i32 s45, s46, s39
	s_and_b32 s39, s45, 0xffc0
	s_sub_i32 s39, s46, s39
	s_sext_i32_i16 s84, s39
	s_lshl_b32 s46, s84, 5
	s_ashr_i32 s39, s38, 31
	s_ashr_i32 s47, s46, 31
	s_cmp_gt_i32 s4, 1
	s_mov_b64 s[70:71], -1
	s_cbranch_scc0 .LBB0_110
	s_lshl_b64 s[68:69], s[38:39], 22
	s_lshl_b64 s[70:71], s[46:47], 11
	s_add_u32 s68, s73, s68
	s_addc_u32 s69, s74, s69
	s_add_u32 s68, s68, s70
	s_addc_u32 s69, s69, s71
	s_mov_b64 s[70:71], 0
